# speedup vs baseline: 1.0082x; 1.0082x over previous
.LBB2_13:
	s_waitcnt vmcnt(0)
	s_barrier
	v_add_u32_e32 v34, s22, v109
	v_add_u32_e32 v34, 0xffff4000, v34
	v_and_b32_e32 v34, 0xc000, v34
	v_add_u32_e32 v114, 0, v34
	v_add_u32_e32 v38, v114, v106
	v_add_u32_e32 v82, v114, v105
	v_add_u32_e32 v89, v114, v104
	v_add_u32_e32 v90, v114, v103
	ds_read_b128 v[34:37], v38
	ds_read_b128 v[38:41], v38 offset:4096
	ds_read_b128 v[116:119], v82
	ds_read_b128 v[120:123], v82 offset:4096
	ds_read_b128 v[124:127], v89
	s_waitcnt lgkmcnt(3)
	v_mfma_f32_32x32x16_f16 v[50:65], v[34:37], v[78:81], 0
	v_mfma_f32_32x32x16_f16 v[34:49], v[38:41], v[78:81], 0
	s_waitcnt lgkmcnt(2)
	v_mfma_f32_32x32x16_f16 v[50:65], v[116:119], v[74:77], v[50:65]
	ds_read_b128 v[116:119], v89 offset:4096
	s_waitcnt lgkmcnt(2)
	v_mfma_f32_32x32x16_f16 v[34:49], v[120:123], v[74:77], v[34:49]
	ds_read_b128 v[120:123], v90
	s_waitcnt lgkmcnt(2)
	v_mfma_f32_32x32x16_f16 v[50:65], v[124:127], v[70:73], v[50:65]
	ds_read_b128 v[124:127], v90 offset:4096
	s_waitcnt lgkmcnt(2)
	v_mfma_f32_32x32x16_f16 v[34:49], v[116:119], v[70:73], v[34:49]
	s_waitcnt lgkmcnt(1)
	v_mfma_f32_32x32x16_f16 v[50:65], v[120:123], v[66:69], v[50:65]
	s_waitcnt lgkmcnt(0)
	v_mfma_f32_32x32x16_f16 v[34:49], v[124:127], v[66:69], v[34:49]
	s_nop 9
	v_max3_f32 v82, v50, v51, v52
	v_max3_f32 v82, v82, v53, v54
	v_max3_f32 v82, v82, v55, v56
	v_max3_f32 v82, v82, v57, v58
	v_max3_f32 v82, v82, v59, v60
	v_max3_f32 v82, v82, v61, v62
	v_max_f32_e32 v91, v65, v65
	v_max3_f32 v89, v34, v35, v36
	v_max3_f32 v89, v89, v37, v38
	v_max3_f32 v89, v89, v39, v40
	v_max3_f32 v89, v89, v41, v42
	v_max3_f32 v89, v89, v43, v44
	v_max3_f32 v89, v89, v45, v46
	v_max_f32_e32 v90, v49, v49
	v_max3_f32 v82, v82, v63, v64
	v_max3_f32 v89, v89, v47, v48
	v_max_f32_e32 v90, v91, v90
	v_max3_f32 v82, v82, v89, v90
	v_mov_b32_e32 v89, v82
	s_nop 1
	v_permlane32_swap_b32_e32 v82, v89
	v_max_f32_e32 v82, v82, v89
	v_fma_f32 v89, v82, s23, -v88
	v_cmp_lt_f32_e32 vcc, s24, v89
	s_cbranch_vccz .LBB2_16
	v_mul_f32_e32 v82, 0x3e38aa3b, v82
	v_max_f32_e32 v82, v82, v82
	v_max_f32_e32 v89, v88, v88
	v_max_f32_e32 v102, v89, v82
	v_sub_f32_e32 v82, v88, v102
	v_exp_f32_e32 v82, v82
	s_and_saveexec_b64 s[16:17], s[4:5]
	s_cbranch_execz .LBB2_11
	v_lshl_add_u32 v88, v95, 2, v100
	ds_write_b32 v88, v82
	s_branch .LBB2_11
